# speedup vs baseline: 1.0127x; 1.0127x over previous
_Z11gram_kernelPKfPKiS0_S0_S0_S0_S0_S0_S0_S0_S0_Pf:
	s_load_dwordx4 s[24:27], s[0:1], 0x0
	s_load_dwordx2 s[28:29], s[0:1], 0x40
	s_load_dwordx4 s[20:23], s[0:1], 0x30
	s_load_dwordx2 s[60:61], s[0:1], 0x18
	s_load_dwordx2 s[62:63], s[0:1], 0x28
	s_load_dwordx2 s[64:65], s[0:1], 0x48
	s_load_dwordx2 s[66:67], s[0:1], 0x50
	s_ashr_i32 s30, s2, 1
	s_getpc_b64 s[4:5]
	s_and_b32 s4, s4, 0xfffffc00
	v_lshlrev_b32_e32 v10, 7, v0
	v_mov_b32_e32 v11, 0
	s_ashr_i32 s31, s30, 31
	v_lshl_add_u64 v[2:3], s[4:5], 0, v[10:11]
	s_lshl_b64 s[4:5], s[30:31], 14
	v_lshlrev_b32_e32 v246, 2, v0
	v_and_b32_e32 v246, 0x1fc, v246
	v_mov_b32_e32 v250, 0
	s_waitcnt lgkmcnt(0)
	global_load_dword v247, v246, s[60:61]
	global_load_dword v248, v246, s[62:63]
	global_load_dword v249, v246, s[64:65]
	global_load_dword v250, v250, s[66:67]
	s_add_u32 s48, s20, s4
	s_addc_u32 s49, s21, s5
	s_movk_i32 s4, 0xa000
	s_movk_i32 s3, 0xbf
	v_lshl_add_u64 v[4:5], s[48:49], 0, v[10:11]
	s_mov_b32 s5, -1
	v_lshl_add_u64 v[4:5], v[4:5], 0, s[4:5]
	v_cmp_lt_u32_e32 vcc, s3, v0
	s_movk_i32 s3, 0x13f
	s_mov_b64 s[36:37], s[24:25]
	v_cndmask_b32_e32 v3, v3, v5, vcc
	v_cndmask_b32_e32 v2, v2, v4, vcc
	v_cmp_lt_u32_e32 vcc, s3, v0
	s_and_saveexec_b64 s[4:5], vcc
	s_cbranch_execz .LBB0_2
	v_and_b32_e32 v1, 16, v0
	v_mov_b32_e32 v2, s29
	v_mov_b32_e32 v3, s23
	v_cmp_eq_u32_e32 vcc, 0, v1
	s_lshl_b32 s3, s2, 1
	v_mov_b32_e32 v1, s28
	v_cndmask_b32_e32 v3, v2, v3, vcc
	v_mov_b32_e32 v2, s22
	s_and_b32 s3, s3, 0x1f0
	v_cndmask_b32_e32 v2, v1, v2, vcc
	v_and_or_b32 v1, v0, 15, s3
	v_lshlrev_b32_e32 v4, 7, v1
	v_mov_b32_e32 v5, 0
	v_lshl_add_u64 v[2:3], v[2:3], 0, v[4:5]

.LBB0_33:
	v_lshlrev_b32_e32 v180, 2, v215
	v_lshl_add_u32 v180, v214, 4, v180
	global_load_dwordx4 v[184:187], v180, s[64:65]
	global_load_dwordx4 v[188:191], v180, s[64:65] offset:32
	global_load_dwordx4 v[192:195], v180, s[64:65] offset:64
	global_load_dwordx4 v[196:199], v180, s[64:65] offset:96
	s_waitcnt vmcnt(15)
	v_lshl_add_u64 v[34:35], v[46:47], 2, s[48:49]
	v_add_co_u32_e32 v36, vcc, 0x2000, v34
	v_lshlrev_b32_e32 v1, 2, v231
	s_nop 0
	v_addc_co_u32_e32 v37, vcc, 0, v35, vcc
	s_waitcnt lgkmcnt(0)
	global_load_dword v104, v1, s[52:53]
	global_load_dword v100, v1, s[54:55]
	global_load_dwordx4 v[38:41], v[34:35], off
	s_nop 0
	global_load_dwordx4 v[34:37], v[36:37], off
	v_bfe_u32 v0, v0, 6, 2
	s_waitcnt vmcnt(17)
	v_and_b32_e32 v42, 6, v222
	v_lshl_or_b32 v0, v214, 4, v0
	v_mov_b32_e32 v43, 0x10000
	s_waitcnt vmcnt(15)
	v_lshl_or_b32 v103, v220, 3, v43
	v_lshlrev_b32_e32 v42, 1, v42
	v_mul_u32_u24_e32 v0, 0x110, v0
	v_cvt_pk_f16_f32 v2, v18, v2
	v_add3_u32 v18, v103, v42, v0
	v_cvt_pk_f16_f32 v0, v19, v3
	ds_write_b32 v18, v0 offset:1088
	v_cvt_pk_f16_f32 v0, v20, v4
	ds_write_b32 v18, v0 offset:2176
	v_cvt_pk_f16_f32 v0, v21, v5
	ds_write_b32 v18, v0 offset:3264
	v_cvt_pk_f16_f32 v0, v22, v6
	ds_write_b32 v18, v0 offset:8704
	v_cvt_pk_f16_f32 v0, v23, v7
	ds_write_b32 v18, v0 offset:9792
	v_cvt_pk_f16_f32 v0, v24, v8
	ds_write_b32 v18, v0 offset:10880
	v_cvt_pk_f16_f32 v0, v25, v9
	ds_write_b32 v18, v0 offset:11968
	v_cvt_pk_f16_f32 v0, v26, v10
	ds_write_b32 v18, v0 offset:17408
	v_cvt_pk_f16_f32 v0, v27, v11
	ds_write_b32 v18, v0 offset:18496
	v_cvt_pk_f16_f32 v0, v28, v12
	ds_write_b32 v18, v0 offset:19584
	v_cvt_pk_f16_f32 v0, v29, v13
	ds_write_b32 v18, v0 offset:20672
	v_cvt_pk_f16_f32 v0, v30, v14
	ds_write_b32 v18, v0 offset:26112
	v_cvt_pk_f16_f32 v0, v31, v15
	ds_write_b32 v18, v0 offset:27200
	v_cvt_pk_f16_f32 v0, v32, v16
	ds_write_b32 v18, v0 offset:28288
	v_mbcnt_lo_u32_b32 v0, -1, 0
	v_mbcnt_hi_u32_b32 v101, -1, v0
	ds_write_b32 v18, v2
	v_and_b32_e32 v2, 64, v101
	v_xor_b32_e32 v0, 32, v101
	v_add_u32_e32 v2, 64, v2
	v_cmp_lt_i32_e32 vcc, v0, v2
	s_load_dwordx2 s[2:3], s[0:1], 0x48
	s_load_dword s10, s[50:51], 0x0
	v_cndmask_b32_e32 v0, v101, v0, vcc
	v_lshlrev_b32_e32 v102, 2, v0
	ds_bpermute_b32 v0, v102, v217
	v_cmp_gt_u32_e32 vcc, 32, v218
	v_lshlrev_b32_e32 v1, 2, v220
	s_movk_i32 s6, 0x110
	v_cvt_pk_f16_f32 v2, v33, v17
	s_and_b64 s[12:13], s[4:5], vcc
	ds_write_b32 v18, v2 offset:29376
	s_and_saveexec_b64 s[0:1], s[12:13]
	s_cbranch_execz .LBB0_35
	s_waitcnt lgkmcnt(0)
	v_add_f32_e32 v0, v217, v0
	v_cvt_f16_f32_e32 v0, v0
	v_lshlrev_b32_e32 v2, 1, v1
	v_lshlrev_b32_e32 v3, 1, v219
	s_mov_b32 s7, 0x21000
	v_add3_u32 v2, v3, v2, s7
	ds_write_b16 v2, v0

.LBB0_39:
	s_or_b64 exec, exec, s[6:7]
	v_cvt_pk_f16_f32 v17, v118, v119
	v_cvt_pk_f16_f32 v16, v116, v117
	v_add_u32_e32 v20, v103, v105
	v_cvt_pk_f16_f32 v19, v122, v123
	v_cvt_pk_f16_f32 v18, v120, v121
	s_waitcnt lgkmcnt(0)
	s_barrier
	ds_write2_b64 v20, v[16:17], v[18:19] offset1:34
	v_cvt_pk_f16_f32 v17, v126, v127
	v_cvt_pk_f16_f32 v16, v124, v125
	v_cvt_pk_f16_f32 v19, v130, v131
	v_cvt_pk_f16_f32 v18, v128, v129
	ds_write2_b64 v20, v[16:17], v[18:19] offset0:68 offset1:102
	v_cvt_pk_f16_f32 v17, v134, v135
	v_cvt_pk_f16_f32 v16, v132, v133
	v_cvt_pk_f16_f32 v19, v138, v139
	v_cvt_pk_f16_f32 v18, v136, v137
	ds_write2_b64 v20, v[16:17], v[18:19] offset0:136 offset1:170
	v_cvt_pk_f16_f32 v17, v142, v143
	v_cvt_pk_f16_f32 v16, v140, v141
	v_cvt_pk_f16_f32 v19, v146, v147
	v_cvt_pk_f16_f32 v18, v144, v145
	ds_write2_b64 v20, v[16:17], v[18:19] offset0:204 offset1:238
	s_and_saveexec_b64 s[6:7], s[0:1]
	s_cbranch_execz .LBB0_49
	v_lshlrev_b32_e32 v16, 2, v215
	v_mov_b32_e32 v215, 0
	v_mov_b32_e32 v17, v215
	v_lshl_add_u64 v[16:17], s[2:3], 0, v[16:17]
	v_lshlrev_b32_e32 v18, 4, v214
	v_mov_b32_e32 v19, v215
	v_lshl_add_u64 v[34:35], v[16:17], 0, v[18:19]
	v_add_u32_e32 v54, v224, v223
	ds_read_b128 v[34:37], v54
	s_movk_i32 s0, 0x110
	v_mad_u32_u24 v70, v220, s0, v223
	ds_read_b128 v[38:41], v70 offset:34816
	ds_read_b128 v[42:45], v54 offset:32
	ds_read_b128 v[46:49], v70 offset:34848
	v_lshl_or_b32 v32, v222, 12, v32
	v_add_u32_e32 v78, 0x18800, v32
	v_div_scale_f32 v82, s[0:1], s10, s10, 1.0
	v_rcp_f32_e32 v84, v82
	v_div_scale_f32 v83, vcc, 1.0, s10, 1.0
	s_waitcnt vmcnt(0) lgkmcnt(2)
	v_mfma_f32_32x32x16_f16 v[16:31], v[34:37], v[38:41], v[184:199]
	ds_read_b128 v[34:37], v54 offset:64
	ds_read_b128 v[38:41], v70 offset:34880
	s_waitcnt lgkmcnt(2)
	v_mfma_f32_32x32x16_f16 v[16:31], v[42:45], v[46:49], v[16:31]
	ds_read_b128 v[42:45], v54 offset:96
	ds_read_b128 v[46:49], v70 offset:34912
	s_waitcnt lgkmcnt(2)
	v_mfma_f32_32x32x16_f16 v[16:31], v[34:37], v[38:41], v[16:31]
	ds_read_b128 v[32:35], v54 offset:128
	ds_read_b128 v[36:39], v54 offset:160
	ds_read_b128 v[50:53], v54 offset:192
	ds_read_b128 v[54:57], v54 offset:224
	ds_read_b128 v[58:61], v70 offset:34944
	ds_read_b128 v[62:65], v70 offset:34976
	ds_read_b128 v[66:69], v70 offset:35008
	ds_read_b128 v[70:73], v70 offset:35040
	s_waitcnt lgkmcnt(8)
	v_mfma_f32_32x32x16_f16 v[16:31], v[42:45], v[46:49], v[16:31]
	ds_read_b128 v[40:43], v78
	ds_read_b128 v[44:47], v78 offset:16
	ds_read_b128 v[74:77], v78 offset:32
	ds_read_b128 v[78:81], v78 offset:48
	v_fma_f32 v48, -v82, v84, 1.0
	v_fmac_f32_e32 v84, v48, v84
	v_mul_f32_e32 v48, v83, v84
	s_waitcnt lgkmcnt(7)
	v_mfma_f32_32x32x16_f16 v[16:31], v[32:35], v[58:61], v[16:31]
	s_waitcnt lgkmcnt(3)
	v_add_f32_e64 v32, v0, v40
	v_add_f32_e64 v33, v1, v41
	v_add_f32_e64 v0, v42, v2
	v_add_f32_e64 v1, v43, v3
	s_waitcnt lgkmcnt(2)
	v_pk_add_f32 v[2:3], v[4:5], v[44:45]
	v_pk_add_f32 v[4:5], v[46:47], v[6:7]
	s_waitcnt lgkmcnt(1)
	v_pk_add_f32 v[6:7], v[8:9], v[74:75]
	s_waitcnt lgkmcnt(0)
	v_pk_add_f32 v[8:9], v[12:13], v[78:79]
	v_fma_f32 v12, -v82, v48, v83
	v_mfma_f32_32x32x16_f16 v[16:31], v[36:39], v[62:65], v[16:31]
	v_fmac_f32_e32 v48, v12, v84
	v_cvt_pk_f16_f32 v2, v2, v3
	v_cvt_pk_f16_f32 v3, v4, v5
	v_cvt_pk_f16_f32 v1, v0, v1
	v_cvt_pk_f16_f32 v0, v32, v33
	v_fma_f32 v4, -v82, v48, v83
	v_div_fmas_f32 v4, v4, v84, v48
	v_mfma_f32_32x32x16_f16 v[16:31], v[50:53], v[66:69], v[16:31]
	v_add_f32_e64 v40, v76, v10
	v_add_f32_e64 v41, v77, v11
	v_add_f32_e64 v10, v80, v14
	v_add_f32_e64 v11, v81, v15
	v_div_fixup_f32 v4, v4, s10, 1.0
	v_cvt_pk_f16_f32 v34, v8, v9
	v_cvt_pk_f16_f32 v32, v6, v7
	v_cvt_pk_f16_f32 v35, v10, v11
	v_cvt_pk_f16_f32 v33, v40, v41
	v_mfma_f32_32x32x16_f16 v[16:31], v[54:57], v[70:73], v[16:31]
	s_andn2_b64 vcc, exec, s[8:9]
	s_nop 10
	v_mul_f32_e32 v8, v4, v16
	v_mul_f32_e32 v9, v4, v17
	v_mul_f32_e32 v5, v4, v18
	v_mul_f32_e32 v10, v4, v19
	v_mul_f32_e32 v6, v4, v20
	v_mul_f32_e32 v11, v4, v21
	v_mul_f32_e32 v7, v4, v22
	v_mul_f32_e32 v12, v4, v23
	v_mul_f32_e32 v16, v4, v24
	v_mul_f32_e32 v20, v4, v25
	v_mul_f32_e32 v17, v4, v26
	v_mul_f32_e32 v21, v4, v27
	v_mul_f32_e32 v18, v4, v28
	v_mul_f32_e32 v22, v4, v29
	v_mul_f32_e32 v19, v4, v30
	v_mul_f32_e32 v23, v4, v31
	v_cvt_pk_f16_f32 v7, v7, v12
	v_cvt_pk_f16_f32 v6, v6, v11
	v_cvt_pk_f16_f32 v5, v5, v10
	v_cvt_pk_f16_f32 v4, v8, v9
	v_cvt_pk_f16_f32 v19, v19, v23
	v_cvt_pk_f16_f32 v18, v18, v22
	v_mfma_f32_32x32x16_f16 v[0:15], v[0:3], v[4:7], 0
	v_cvt_pk_f16_f32 v17, v17, v21
	v_cvt_pk_f16_f32 v16, v16, v20
	s_nop 1
	v_mfma_f32_32x32x16_f16 v[0:15], v[32:35], v[16:19], v[0:15]
	s_cbranch_vccnz .LBB0_48
	v_lshlrev_b32_e32 v16, 7, v220
	v_lshl_or_b32 v16, v222, 12, v16
	v_mov_b32_e32 v17, v215
	s_add_i32 s33, s33, s46
	v_lshlrev_b32_e32 v22, 2, v214
	v_lshl_add_u64 v[16:17], v[16:17], 2, s[44:45]
	v_add_u32_e32 v18, s33, v214
	s_mov_b64 s[0:1], 0
	s_movk_i32 s10, 0x3fd
	v_mov_b32_e32 v23, v215
	s_branch .LBB0_43

	.amdhsa_kernel _Z11gram_kernelPKfPKiS0_S0_S0_S0_S0_S0_S0_S0_S0_Pf
		.amdhsa_group_segment_fixed_size 135456
		.amdhsa_private_segment_fixed_size 0
		.amdhsa_kernarg_size 96
		.amdhsa_user_sgpr_count 2
		.amdhsa_user_sgpr_dispatch_ptr 0
		.amdhsa_user_sgpr_queue_ptr 0
		.amdhsa_user_sgpr_kernarg_segment_ptr 1
		.amdhsa_user_sgpr_dispatch_id 0
		.amdhsa_user_sgpr_kernarg_preload_length 0
		.amdhsa_user_sgpr_kernarg_preload_offset 0
		.amdhsa_user_sgpr_private_segment_size 0
		.amdhsa_uses_dynamic_stack 0
		.amdhsa_enable_private_segment 0
		.amdhsa_system_sgpr_workgroup_id_x 1
		.amdhsa_system_sgpr_workgroup_id_y 0
		.amdhsa_system_sgpr_workgroup_id_z 0
		.amdhsa_system_sgpr_workgroup_info 0
		.amdhsa_system_vgpr_workitem_id 0
		.amdhsa_next_free_vgpr 251
		.amdhsa_next_free_sgpr 96
		.amdhsa_accum_offset 252
		.amdhsa_reserve_vcc 1
		.amdhsa_float_round_mode_32 0
		.amdhsa_float_round_mode_16_64 0
		.amdhsa_float_denorm_mode_32 3
		.amdhsa_float_denorm_mode_16_64 3
		.amdhsa_dx10_clamp 1
		.amdhsa_ieee_mode 1
		.amdhsa_fp16_overflow 0
		.amdhsa_tg_split 0
		.amdhsa_exception_fp_ieee_invalid_op 0
		.amdhsa_exception_fp_denorm_src 0
		.amdhsa_exception_fp_ieee_div_zero 0
		.amdhsa_exception_fp_ieee_overflow 0
		.amdhsa_exception_fp_ieee_underflow 0
		.amdhsa_exception_fp_ieee_inexact 0
		.amdhsa_exception_int_div_zero 0
	.end_amdhsa_kernel

amdhsa.kernels:
  - .agpr_count:     0
    .args:
      - .actual_access:  read_only
        .address_space:  global
        .offset:         0
        .size:           8
        .value_kind:     global_buffer
      - .actual_access:  read_only
        .address_space:  global
        .offset:         8
        .size:           8
        .value_kind:     global_buffer
      - .actual_access:  read_only
        .address_space:  global
        .offset:         16
        .size:           8
        .value_kind:     global_buffer
      - .actual_access:  read_only
        .address_space:  global
        .offset:         24
        .size:           8
        .value_kind:     global_buffer
      - .actual_access:  read_only
        .address_space:  global
        .offset:         32
        .size:           8
        .value_kind:     global_buffer
      - .actual_access:  read_only
        .address_space:  global
        .offset:         40
        .size:           8
        .value_kind:     global_buffer
      - .address_space:  global
        .offset:         48
        .size:           8
        .value_kind:     global_buffer
      - .address_space:  global
        .offset:         56
        .size:           8
        .value_kind:     global_buffer
      - .address_space:  global
        .offset:         64
        .size:           8
        .value_kind:     global_buffer
      - .actual_access:  read_only
        .address_space:  global
        .offset:         72
        .size:           8
        .value_kind:     global_buffer
      - .actual_access:  read_only
        .address_space:  global
        .offset:         80
        .size:           8
        .value_kind:     global_buffer
      - .actual_access:  write_only
        .address_space:  global
        .offset:         88
        .size:           8
        .value_kind:     global_buffer
    .group_segment_fixed_size: 135456
    .kernarg_segment_align: 8
    .kernarg_segment_size: 96
    .language:       OpenCL C
    .language_version:
      - 2
      - 0
    .max_flat_workgroup_size: 512
    .name:           _Z11gram_kernelPKfPKiS0_S0_S0_S0_S0_S0_S0_S0_S0_Pf
    .private_segment_fixed_size: 0
    .sgpr_count:     66
    .sgpr_spill_count: 0
    .symbol:         _Z11gram_kernelPKfPKiS0_S0_S0_S0_S0_S0_S0_S0_S0_Pf.kd
    .uniform_work_group_size: 1
    .uses_dynamic_stack: false
    .vgpr_count:     251
    .vgpr_spill_count: 0
    .wavefront_size: 64
  - .agpr_count:     0
    .args:
      - .actual_access:  read_only
        .address_space:  global
        .offset:         0
        .size:           8
        .value_kind:     global_buffer
      - .actual_access:  read_only
        .address_space:  global
        .offset:         8
        .size:           8
        .value_kind:     global_buffer
      - .actual_access:  write_only
        .address_space:  global
        .offset:         16
        .size:           8
        .value_kind:     global_buffer
    .group_segment_fixed_size: 0
    .kernarg_segment_align: 8
    .kernarg_segment_size: 24
    .language:       OpenCL C
    .language_version:
      - 2
      - 0
    .max_flat_workgroup_size: 256
    .name:           _Z10fin_kernelPKfS0_Pf
    .private_segment_fixed_size: 0
    .sgpr_count:     16
    .sgpr_spill_count: 0
    .symbol:         _Z10fin_kernelPKfS0_Pf.kd
    .uniform_work_group_size: 1
    .uses_dynamic_stack: false
    .vgpr_count:     50
    .vgpr_spill_count: 0
    .wavefront_size: 64
